# grid barrier: non-leader workgroups poll the cross-XCC generation word directly, per-XCC generation bump by the leader removed
# baseline (speedup 1.0000x reference)
.LBB0_278:
	s_or_b64 exec, exec, s[8:9]
	v_cvt_f32_u32_e32 v6, v4
	s_waitcnt vmcnt(0)
	v_readfirstlane_b32 s6, v5
	v_sub_u32_e32 v5, 0, v4
	v_rcp_iflag_f32_e32 v6, v6
	v_add_u32_e32 v7, s6, v3
	v_mul_f32_e32 v6, 0x4f7ffffe, v6
	v_cvt_u32_f32_e32 v6, v6
	v_mul_lo_u32 v3, v5, v6
	v_mul_hi_u32 v3, v6, v3
	v_add_u32_e32 v3, v6, v3
	v_mul_hi_u32 v3, v7, v3
	v_mul_lo_u32 v5, v3, v4
	v_sub_u32_e32 v5, v7, v5
	v_add_u32_e32 v6, 1, v3
	v_cmp_ge_u32_e32 vcc, v5, v4
	s_nop 1
	v_cndmask_b32_e32 v3, v3, v6, vcc
	v_sub_u32_e32 v6, v5, v4
	v_cndmask_b32_e32 v5, v5, v6, vcc
	v_add_u32_e32 v6, 1, v3
	v_cmp_ge_u32_e32 vcc, v5, v4
	v_add_u32_e32 v5, 1, v7
	s_nop 0
	v_cndmask_b32_e32 v3, v3, v6, vcc
	v_mul_lo_u32 v6, v4, v3
	v_add_u32_e32 v4, v6, v4
	v_cmp_ne_u32_e32 vcc, v5, v4
	s_and_saveexec_b64 s[6:7], vcc
	s_xor_b64 s[6:7], exec, s[6:7]
	s_cbranch_execz .LBB0_292
	s_waitcnt lgkmcnt(0)
	s_add_u32 s12, s68, 0x7500
	s_addc_u32 s13, s69, 0
	v_mov_b32_e32 v2, 0
	global_load_dword v2, v2, s[12:13] sc1
	s_waitcnt vmcnt(0)
	v_cmp_eq_u32_e32 vcc, v2, v3
	s_and_saveexec_b64 s[8:9], vcc
	s_cbranch_execz .LBB0_291
	s_add_u32 s10, s68, 0x4200
	s_addc_u32 s11, s69, 0
	s_mov_b32 s33, 1
	s_mov_b64 s[14:15], 0
	v_mov_b32_e32 v2, 0
	s_branch .LBB0_282

.LBB0_309:
	s_or_b64 exec, exec, s[6:7]
	s_mov_b64 s[6:7], exec
	v_mbcnt_lo_u32_b32 v2, s6, 0
	v_mbcnt_hi_u32_b32 v2, s7, v2
	v_cmp_eq_u32_e32 vcc, 0, v2
	s_waitcnt vmcnt(0)
	buffer_inv sc1
	s_and_saveexec_b64 s[8:9], vcc
	s_cbranch_execz .LBB0_311
	s_bcnt1_i32_b64 s6, s[6:7]
	v_mov_b32_e32 v2, 0x2000
	v_mov_b32_e32 v3, s6
	s_nop 0

.LBB0_858:
	s_or_b64 exec, exec, s[8:9]
	v_cvt_f32_u32_e32 v6, v4
	s_waitcnt vmcnt(0)
	v_readfirstlane_b32 s6, v5
	v_sub_u32_e32 v5, 0, v4
	v_rcp_iflag_f32_e32 v6, v6
	v_add_u32_e32 v7, s6, v3
	v_mul_f32_e32 v6, 0x4f7ffffe, v6
	v_cvt_u32_f32_e32 v6, v6
	v_mul_lo_u32 v3, v5, v6
	v_mul_hi_u32 v3, v6, v3
	v_add_u32_e32 v3, v6, v3
	v_mul_hi_u32 v3, v7, v3
	v_mul_lo_u32 v5, v3, v4
	v_sub_u32_e32 v5, v7, v5
	v_add_u32_e32 v6, 1, v3
	v_cmp_ge_u32_e32 vcc, v5, v4
	s_nop 1
	v_cndmask_b32_e32 v3, v3, v6, vcc
	v_sub_u32_e32 v6, v5, v4
	v_cndmask_b32_e32 v5, v5, v6, vcc
	v_add_u32_e32 v6, 1, v3
	v_cmp_ge_u32_e32 vcc, v5, v4
	v_add_u32_e32 v5, 1, v7
	s_nop 0
	v_cndmask_b32_e32 v3, v3, v6, vcc
	v_mul_lo_u32 v6, v4, v3
	v_add_u32_e32 v4, v6, v4
	v_cmp_ne_u32_e32 vcc, v5, v4
	s_and_saveexec_b64 s[6:7], vcc
	s_xor_b64 s[6:7], exec, s[6:7]
	s_cbranch_execz .LBB0_872
	s_waitcnt lgkmcnt(0)
	s_add_u32 s12, s68, 0x7500
	s_addc_u32 s13, s69, 0
	v_mov_b32_e32 v2, 0
	global_load_dword v2, v2, s[12:13] sc1
	s_waitcnt vmcnt(0)
	v_cmp_eq_u32_e32 vcc, v2, v3
	s_and_saveexec_b64 s[8:9], vcc
	s_cbranch_execz .LBB0_871
	s_add_u32 s10, s68, 0x4200
	s_addc_u32 s11, s69, 0
	s_mov_b32 s26, 1
	s_mov_b64 s[14:15], 0
	v_mov_b32_e32 v2, 0
	s_branch .LBB0_862

.LBB0_1293:
	s_or_b64 exec, exec, s[8:9]
	v_cvt_f32_u32_e32 v5, v3
	s_waitcnt vmcnt(0)
	v_readfirstlane_b32 s6, v4
	v_sub_u32_e32 v4, 0, v3
	v_rcp_iflag_f32_e32 v5, v5
	v_add_u32_e32 v6, s6, v2
	v_mul_f32_e32 v5, 0x4f7ffffe, v5
	v_cvt_u32_f32_e32 v5, v5
	v_mul_lo_u32 v2, v4, v5
	v_mul_hi_u32 v2, v5, v2
	v_add_u32_e32 v2, v5, v2
	v_mul_hi_u32 v2, v6, v2
	v_mul_lo_u32 v4, v2, v3
	v_sub_u32_e32 v4, v6, v4
	v_add_u32_e32 v5, 1, v2
	v_cmp_ge_u32_e32 vcc, v4, v3
	s_nop 1
	v_cndmask_b32_e32 v2, v2, v5, vcc
	v_sub_u32_e32 v5, v4, v3
	v_cndmask_b32_e32 v4, v4, v5, vcc
	v_add_u32_e32 v5, 1, v2
	v_cmp_ge_u32_e32 vcc, v4, v3
	v_add_u32_e32 v4, 1, v6
	s_nop 0
	v_cndmask_b32_e32 v2, v2, v5, vcc
	v_mul_lo_u32 v5, v3, v2
	v_add_u32_e32 v3, v5, v3
	v_cmp_ne_u32_e32 vcc, v4, v3
	s_and_saveexec_b64 s[6:7], vcc
	s_xor_b64 s[6:7], exec, s[6:7]
	s_cbranch_execz .LBB0_1307
	s_waitcnt lgkmcnt(0)
	s_add_u32 s12, s68, 0x7500
	s_addc_u32 s13, s69, 0
	v_mov_b32_e32 v1, 0
	global_load_dword v1, v1, s[12:13] sc1
	s_waitcnt vmcnt(0)
	v_cmp_eq_u32_e32 vcc, v1, v2
	s_and_saveexec_b64 s[8:9], vcc
	s_cbranch_execz .LBB0_1306
	s_add_u32 s10, s68, 0x4200
	s_addc_u32 s11, s69, 0
	s_mov_b32 s24, 1
	s_mov_b64 s[14:15], 0
	v_mov_b32_e32 v1, 0
	s_branch .LBB0_1297

.LBB0_1324:
	s_or_b64 exec, exec, s[6:7]
	s_mov_b64 s[6:7], exec
	v_mbcnt_lo_u32_b32 v1, s6, 0
	v_mbcnt_hi_u32_b32 v1, s7, v1
	v_cmp_eq_u32_e32 vcc, 0, v1
	s_waitcnt vmcnt(0)
	buffer_inv sc1
	s_and_saveexec_b64 s[8:9], vcc
	s_cbranch_execz .LBB0_1326
	s_bcnt1_i32_b64 s6, s[6:7]
	v_mov_b32_e32 v1, 0x2000
	v_mov_b32_e32 v2, s6
	s_nop 0

.LBB0_1378:
	s_or_b64 exec, exec, s[12:13]
	v_cvt_f32_u32_e32 v5, v3
	s_waitcnt vmcnt(0)
	v_readfirstlane_b32 s5, v4
	v_sub_u32_e32 v4, 0, v3
	v_rcp_iflag_f32_e32 v5, v5
	v_add_u32_e32 v6, s5, v2
	v_mul_f32_e32 v5, 0x4f7ffffe, v5
	v_cvt_u32_f32_e32 v5, v5
	v_mul_lo_u32 v2, v4, v5
	v_mul_hi_u32 v2, v5, v2
	v_add_u32_e32 v2, v5, v2
	v_mul_hi_u32 v2, v6, v2
	v_mul_lo_u32 v4, v2, v3
	v_sub_u32_e32 v4, v6, v4
	v_add_u32_e32 v5, 1, v2
	v_cmp_ge_u32_e32 vcc, v4, v3
	s_nop 1
	v_cndmask_b32_e32 v2, v2, v5, vcc
	v_sub_u32_e32 v5, v4, v3
	v_cndmask_b32_e32 v4, v4, v5, vcc
	v_add_u32_e32 v5, 1, v2
	v_cmp_ge_u32_e32 vcc, v4, v3
	v_add_u32_e32 v4, 1, v6
	s_nop 0
	v_cndmask_b32_e32 v2, v2, v5, vcc
	v_mul_lo_u32 v5, v3, v2
	v_add_u32_e32 v3, v5, v3
	v_cmp_ne_u32_e32 vcc, v4, v3
	s_and_saveexec_b64 s[10:11], vcc
	s_xor_b64 s[10:11], exec, s[10:11]
	s_cbranch_execz .LBB0_1392
	s_waitcnt lgkmcnt(0)
	s_add_u32 s16, s68, 0x7500
	s_addc_u32 s17, s69, 0
	v_mov_b32_e32 v1, 0
	global_load_dword v1, v1, s[16:17] sc1
	s_waitcnt vmcnt(0)
	v_cmp_eq_u32_e32 vcc, v1, v2
	s_and_saveexec_b64 s[12:13], vcc
	s_cbranch_execz .LBB0_1391
	s_add_u32 s14, s68, 0x4200
	s_addc_u32 s15, s69, 0
	s_mov_b32 s5, 1
	s_mov_b64 s[18:19], 0
	v_mov_b32_e32 v1, 0
	s_branch .LBB0_1382

.LBB0_1409:
	s_or_b64 exec, exec, s[10:11]
	s_mov_b64 s[10:11], exec
	v_mbcnt_lo_u32_b32 v1, s10, 0
	v_mbcnt_hi_u32_b32 v1, s11, v1
	v_cmp_eq_u32_e32 vcc, 0, v1
	s_waitcnt vmcnt(0)
	buffer_inv sc1
	s_and_saveexec_b64 s[12:13], vcc
	s_cbranch_execz .LBB0_1411
	s_bcnt1_i32_b64 s5, s[10:11]
	v_mov_b32_e32 v1, 0x2000
	v_mov_b32_e32 v2, s5
	s_nop 0

.LBB0_1715:
	s_or_b64 exec, exec, s[14:15]
	v_cvt_f32_u32_e32 v5, v3
	s_waitcnt vmcnt(0)
	v_readfirstlane_b32 s12, v4
	v_sub_u32_e32 v4, 0, v3
	v_rcp_iflag_f32_e32 v5, v5
	v_add_u32_e32 v6, s12, v2
	v_mul_f32_e32 v5, 0x4f7ffffe, v5
	v_cvt_u32_f32_e32 v5, v5
	v_mul_lo_u32 v2, v4, v5
	v_mul_hi_u32 v2, v5, v2
	v_add_u32_e32 v2, v5, v2
	v_mul_hi_u32 v2, v6, v2
	v_mul_lo_u32 v4, v2, v3
	v_sub_u32_e32 v4, v6, v4
	v_add_u32_e32 v5, 1, v2
	v_cmp_ge_u32_e32 vcc, v4, v3
	s_nop 1
	v_cndmask_b32_e32 v2, v2, v5, vcc
	v_sub_u32_e32 v5, v4, v3
	v_cndmask_b32_e32 v4, v4, v5, vcc
	v_add_u32_e32 v5, 1, v2
	v_cmp_ge_u32_e32 vcc, v4, v3
	v_add_u32_e32 v4, 1, v6
	s_nop 0
	v_cndmask_b32_e32 v2, v2, v5, vcc
	v_mul_lo_u32 v5, v3, v2
	v_add_u32_e32 v3, v5, v3
	v_cmp_ne_u32_e32 vcc, v4, v3
	s_and_saveexec_b64 s[12:13], vcc
	s_xor_b64 s[12:13], exec, s[12:13]
	s_cbranch_execz .LBB0_1729
	s_waitcnt lgkmcnt(0)
	s_add_u32 s18, s68, 0x7500
	s_addc_u32 s19, s69, 0
	v_mov_b32_e32 v1, 0
	global_load_dword v1, v1, s[18:19] sc1
	s_waitcnt vmcnt(0)
	v_cmp_eq_u32_e32 vcc, v1, v2
	s_and_saveexec_b64 s[14:15], vcc
	s_cbranch_execz .LBB0_1728
	s_add_u32 s16, s68, 0x4200
	s_addc_u32 s17, s69, 0
	s_mov_b32 s30, 1
	s_mov_b64 s[20:21], 0
	v_mov_b32_e32 v1, 0
	s_branch .LBB0_1719

.LBB0_1746:
	s_or_b64 exec, exec, s[12:13]
	s_mov_b64 s[12:13], exec
	v_mbcnt_lo_u32_b32 v1, s12, 0
	v_mbcnt_hi_u32_b32 v1, s13, v1
	v_cmp_eq_u32_e32 vcc, 0, v1
	s_waitcnt vmcnt(0)
	buffer_inv sc1
	s_and_saveexec_b64 s[14:15], vcc
	s_cbranch_execz .LBB0_1748
	s_bcnt1_i32_b64 s12, s[12:13]
	v_mov_b32_e32 v1, 0x2000
	v_mov_b32_e32 v2, s12
	s_nop 0

.LBB0_1780:
	s_or_b64 exec, exec, s[6:7]
	v_cvt_f32_u32_e32 v5, v3
	s_waitcnt vmcnt(0)
	v_readfirstlane_b32 s4, v4
	v_sub_u32_e32 v4, 0, v3
	v_rcp_iflag_f32_e32 v5, v5
	v_add_u32_e32 v6, s4, v2
	v_mul_f32_e32 v5, 0x4f7ffffe, v5
	v_cvt_u32_f32_e32 v5, v5
	v_mul_lo_u32 v2, v4, v5
	v_mul_hi_u32 v2, v5, v2
	v_add_u32_e32 v2, v5, v2
	v_mul_hi_u32 v2, v6, v2
	v_mul_lo_u32 v4, v2, v3
	v_sub_u32_e32 v4, v6, v4
	v_add_u32_e32 v5, 1, v2
	v_cmp_ge_u32_e32 vcc, v4, v3
	s_nop 1
	v_cndmask_b32_e32 v2, v2, v5, vcc
	v_sub_u32_e32 v5, v4, v3
	v_cndmask_b32_e32 v4, v4, v5, vcc
	v_add_u32_e32 v5, 1, v2
	v_cmp_ge_u32_e32 vcc, v4, v3
	v_add_u32_e32 v4, 1, v6
	s_nop 0
	v_cndmask_b32_e32 v2, v2, v5, vcc
	v_mul_lo_u32 v5, v3, v2
	v_add_u32_e32 v3, v5, v3
	v_cmp_ne_u32_e32 vcc, v4, v3
	s_and_saveexec_b64 s[4:5], vcc
	s_xor_b64 s[4:5], exec, s[4:5]
	s_cbranch_execz .LBB0_1794
	s_waitcnt lgkmcnt(0)
	s_add_u32 s10, s68, 0x7500
	s_addc_u32 s11, s69, 0
	v_mov_b32_e32 v1, 0
	global_load_dword v1, v1, s[10:11] sc1
	s_waitcnt vmcnt(0)
	v_cmp_eq_u32_e32 vcc, v1, v2
	s_and_saveexec_b64 s[6:7], vcc
	s_cbranch_execz .LBB0_1793
	s_add_u32 s8, s68, 0x4200
	s_addc_u32 s9, s69, 0
	s_mov_b32 s24, 1
	s_mov_b64 s[12:13], 0
	v_mov_b32_e32 v1, 0
	s_branch .LBB0_1784

.LBB0_1811:
	s_or_b64 exec, exec, s[4:5]
	s_mov_b64 s[4:5], exec
	v_mbcnt_lo_u32_b32 v1, s4, 0
	v_mbcnt_hi_u32_b32 v1, s5, v1
	v_cmp_eq_u32_e32 vcc, 0, v1
	s_waitcnt vmcnt(0)
	buffer_inv sc1
	s_and_saveexec_b64 s[6:7], vcc
	s_cbranch_execz .LBB0_1813
	s_bcnt1_i32_b64 s4, s[4:5]
	v_mov_b32_e32 v1, 0x2000
	v_mov_b32_e32 v2, s4
	s_nop 0
